# waves 4-7 issue their first K loads after barrier2 (behind waves 0-3 in the store path) instead of after barrier1
# speedup vs baseline: 1.0338x; 1.0071x over previous
.Lka_late:
	s_nop 9
	v_mul_f32_e64 v0, s18, v0
	v_mul_f32_e64 v1, s19, v1
	v_mul_f32_e64 v2, s18, v2
	v_mul_f32_e64 v3, s19, v3
	v_pk_mul_f32 v[16:17], s[18:19], v[16:17]
	v_pk_mul_f32 v[18:19], s[18:19], v[18:19]
	ds_write_b128 v164, v[0:3]
	ds_write_b128 v164, v[16:19] offset:128
	v_pk_mul_f32 v[0:1], s[18:19], v[4:5]
	v_pk_mul_f32 v[2:3], s[18:19], v[6:7]
	v_pk_mul_f32 v[4:5], s[18:19], v[20:21]
	v_pk_mul_f32 v[6:7], s[18:19], v[22:23]
	ds_write_b128 v164, v[0:3] offset:32
	ds_write_b128 v164, v[4:7] offset:160
	v_pk_mul_f32 v[0:1], s[18:19], v[8:9]
	v_pk_mul_f32 v[2:3], s[18:19], v[10:11]
	v_pk_mul_f32 v[4:5], s[18:19], v[24:25]
	v_pk_mul_f32 v[6:7], s[18:19], v[26:27]
	ds_write_b128 v164, v[0:3] offset:64
	ds_write_b128 v164, v[4:7] offset:192
	v_pk_mul_f32 v[0:1], s[18:19], v[12:13]
	v_pk_mul_f32 v[2:3], s[18:19], v[14:15]
	v_pk_mul_f32 v[4:5], s[18:19], v[28:29]
	v_pk_mul_f32 v[6:7], s[18:19], v[30:31]
	ds_write_b128 v164, v[0:3] offset:96
	ds_write_b128 v164, v[4:7] offset:224
	s_waitcnt lgkmcnt(0)
	s_barrier
	ds_read2_b32 v[0:1], v235 offset1:32
	ds_read2_b32 v[2:3], v235 offset0:64 offset1:96
	ds_read2_b32 v[4:5], v235 offset0:128 offset1:160
	ds_read2_b32 v[6:7], v235 offset0:192 offset1:224
	ds_read2_b32 v[10:11], v236 offset0:128 offset1:160
	ds_read2_b32 v[16:17], v165 offset1:32
	ds_write_b128 v232, v[128:131]
	s_waitcnt lgkmcnt(6)
	v_max_f32_e32 v8, v1, v1
	v_max_f32_e32 v9, v0, v0
	v_max_f32_e32 v8, v9, v8
	s_waitcnt lgkmcnt(5)
	v_max3_f32 v8, v8, v2, v3
	s_waitcnt lgkmcnt(4)
	v_max3_f32 v8, v8, v4, v5
	s_waitcnt lgkmcnt(3)
	v_max3_f32 v14, v8, v6, v7
	ds_read2_b32 v[8:9], v236 offset1:32
	v_sub_f32_e32 v0, v0, v14
	v_sub_f32_e32 v1, v1, v14
	v_exp_f32_e32 v0, v0
	v_exp_f32_e32 v1, v1
	v_sub_f32_e32 v4, v4, v14
	v_sub_f32_e32 v5, v5, v14
	v_exp_f32_e32 v4, v4
	v_exp_f32_e32 v5, v5
	s_waitcnt lgkmcnt(0)
	v_pk_mul_f32 v[0:1], v[8:9], v[0:1]
	ds_read2_b32 v[8:9], v236 offset0:64 offset1:96
	v_sub_f32_e32 v2, v2, v14
	v_sub_f32_e32 v3, v3, v14
	v_exp_f32_e32 v2, v2
	v_exp_f32_e32 v3, v3
	ds_read2_b32 v[12:13], v236 offset0:192 offset1:224
	v_sub_f32_e32 v6, v6, v14
	v_sub_f32_e32 v7, v7, v14
	v_pk_mul_f32 v[18:19], v[10:11], v[4:5]
	v_sub_f32_e32 v4, v247, v14
	ds_read2_b32 v[22:23], v165 offset0:64 offset1:96
	ds_read2_b32 v[24:25], v165 offset0:128 offset1:160
	ds_read2_b32 v[26:27], v165 offset0:192 offset1:224
	v_exp_f32_e32 v6, v6
	v_exp_f32_e32 v7, v7
	v_exp_f32_e32 v34, v4
	v_max_f32_e32 v4, v17, v17
	v_max_f32_e32 v5, v16, v16
	v_add_f32_e32 v0, 0, v0
	s_waitcnt lgkmcnt(4)
	v_pk_mul_f32 v[2:3], v[8:9], v[2:3]
	v_max_f32_e32 v4, v5, v4
	v_add_f32_e32 v0, v0, v1
	s_waitcnt lgkmcnt(2)
	v_max3_f32 v4, v4, v22, v23
	v_add_f32_e32 v0, v0, v2
	s_waitcnt lgkmcnt(1)
	v_max3_f32 v4, v4, v24, v25
	v_add_f32_e32 v0, v0, v3
	v_pk_mul_f32 v[20:21], v[12:13], v[6:7]
	s_waitcnt lgkmcnt(0)
	v_max3_f32 v35, v4, v26, v27
	v_add_f32_e32 v18, v0, v18
	ds_read_b128 v[0:3], v245
	ds_read_b128 v[4:7], v237
	v_sub_f32_e32 v8, v16, v35
	v_exp_f32_e32 v16, v8
	ds_read2_b32 v[28:29], v242 offset1:32
	ds_read_b128 v[8:11], v245 offset:34816
	ds_read_b128 v[12:15], v245 offset:60928
	s_min_u32 s57, s57, 5
	s_waitcnt lgkmcnt(3)
	v_pk_add_f32 v[0:1], v[0:1], v[4:5]
	v_pk_add_f32 v[2:3], v[2:3], v[6:7]
	v_pk_fma_f32 v[30:31], v[16:17], v[0:1], 0 op_sel_hi:[0,1,0]
	v_sub_f32_e32 v0, v17, v35
	v_pk_fma_f32 v[32:33], v[16:17], v[2:3], 0 op_sel_hi:[0,1,0]
	v_exp_f32_e32 v17, v0
	v_add_f32_e32 v0, v18, v19
	v_add_f32_e32 v0, v0, v20
	v_add_f32_e32 v36, v0, v21
	ds_read_b128 v[0:3], v245 offset:8704
	ds_read_b128 v[4:7], v245 offset:17408
	s_waitcnt lgkmcnt(4)
	v_pk_mul_f32 v[18:19], v[28:29], v[16:17]
	v_sub_f32_e32 v16, v22, v35
	v_exp_f32_e32 v16, v16
	v_add_f32_e32 v20, 0, v18
	v_mov_b32_e32 v18, v17
	s_waitcnt lgkmcnt(1)
	v_pk_fma_f32 v[0:1], v[18:19], v[0:1], v[30:31] op_sel_hi:[0,1,1]
	v_pk_fma_f32 v[2:3], v[18:19], v[2:3], v[32:33] op_sel_hi:[0,1,1]
	s_waitcnt lgkmcnt(0)
	v_pk_fma_f32 v[4:5], v[16:17], v[4:5], v[0:1] op_sel_hi:[0,1,1]
	v_sub_f32_e32 v0, v23, v35
	v_pk_fma_f32 v[6:7], v[16:17], v[6:7], v[2:3] op_sel_hi:[0,1,1]
	v_exp_f32_e32 v17, v0
	v_add_f32_e32 v21, v20, v19
	ds_read_b128 v[0:3], v245 offset:26112
	ds_read2_b32 v[18:19], v242 offset0:64 offset1:96
	v_sub_f32_e32 v22, v24, v35
	v_exp_f32_e32 v22, v22
	v_mov_b32_e32 v20, v17
	s_waitcnt lgkmcnt(1)
	v_pk_fma_f32 v[0:1], v[20:21], v[0:1], v[4:5] op_sel_hi:[0,1,1]
	v_pk_fma_f32 v[2:3], v[20:21], v[2:3], v[6:7] op_sel_hi:[0,1,1]
	ds_read2_b32 v[4:5], v242 offset0:128 offset1:160
	v_pk_fma_f32 v[8:9], v[22:23], v[8:9], v[0:1] op_sel_hi:[0,1,1]
	v_sub_f32_e32 v0, v25, v35
	v_pk_fma_f32 v[10:11], v[22:23], v[10:11], v[2:3] op_sel_hi:[0,1,1]
	v_exp_f32_e32 v23, v0
	s_waitcnt lgkmcnt(1)
	v_pk_mul_f32 v[0:1], v[18:19], v[16:17]
	s_lshl_b32 s58, s58, 18
	v_add_f32_e32 v0, v21, v0
	v_add_f32_e32 v2, v0, v1
	s_waitcnt lgkmcnt(0)
	v_pk_mul_f32 v[0:1], v[4:5], v[22:23]
	v_sub_f32_e32 v4, v26, v35
	v_add_f32_e32 v0, v2, v0
	v_add_f32_e32 v17, v0, v1
	ds_read_b128 v[0:3], v245 offset:43520
	v_exp_f32_e32 v18, v4
	ds_read2_b32 v[20:21], v242 offset0:192 offset1:224
	v_sub_f32_e32 v4, v27, v35
	v_exp_f32_e32 v19, v4
	ds_read_b128 v[4:7], v245 offset:52224
	v_mov_b32_e32 v16, v23
	s_waitcnt lgkmcnt(2)
	v_pk_fma_f32 v[0:1], v[16:17], v[0:1], v[8:9] op_sel_hi:[0,1,1]
	s_waitcnt lgkmcnt(1)
	v_pk_mul_f32 v[8:9], v[20:21], v[18:19]
	v_pk_fma_f32 v[2:3], v[16:17], v[2:3], v[10:11] op_sel_hi:[0,1,1]
	v_add_f32_e32 v8, v17, v8
	v_add_f32_e32 v8, v8, v9
	s_waitcnt lgkmcnt(0)
	v_pk_fma_f32 v[0:1], v[18:19], v[4:5], v[0:1] op_sel_hi:[0,1,1]
	v_div_scale_f32 v5, s[60:61], v8, v8, 1.0
	v_pk_fma_f32 v[2:3], v[18:19], v[6:7], v[2:3] op_sel_hi:[0,1,1]
	v_rcp_f32_e32 v6, v5
	v_mov_b32_e32 v4, v19
	v_pk_fma_f32 v[2:3], v[4:5], v[14:15], v[2:3] op_sel_hi:[0,1,1]
	v_pk_fma_f32 v[0:1], v[4:5], v[12:13], v[0:1] op_sel_hi:[0,1,1]
	v_fma_f32 v4, -v5, v6, 1.0
	v_fmac_f32_e32 v6, v4, v6
	v_div_scale_f32 v4, vcc, 1.0, v8, 1.0
	v_mul_f32_e32 v7, v4, v6
	v_fma_f32 v9, -v5, v7, v4
	v_fmac_f32_e32 v7, v9, v6
	v_fma_f32 v4, -v5, v7, v4
	v_div_fmas_f32 v4, v4, v6, v7
	s_lshl_b32 s60, s56, 19
	s_lshl_b32 s61, s55, 13
	v_div_fixup_f32 v4, v4, v8, 1.0
	s_add_i32 s60, s60, s61
	v_pk_mul_f32 v[2:3], v[2:3], v[4:5] op_sel_hi:[1,0]
	v_pk_mul_f32 v[0:1], v[0:1], v[4:5] op_sel_hi:[1,0]
	v_or_b32_e32 v4, s60, v230
	s_lshl_b32 s60, s57, 2
	s_add_i32 s60, s60, 8
	s_and_b32 s60, s60, 56
	s_and_b32 s57, s57, 1
	s_or_b32 s60, s60, s27
	s_or_b32 s57, s57, s28
	s_lshl_b32 s60, s60, 19
	s_lshl_b32 s57, s57, 13
	s_add_i32 s60, s60, s57
	s_or_b32 s62, s39, s59
	s_lshl_b32 s62, s62, 12
	global_store_dwordx4 v4, v[0:3], s[8:9] nt
	v_mov_b32_e32 v252, v34
	v_mov_b32_e32 v253, v36
	v_or_b32_e32 v0, s60, v230
	s_barrier
	global_load_dwordx4 v[128:131], v0, s[4:5]
	s_cmp_lt_u32 s31, 0x200
	s_cbranch_scc1 .Lka_done
	s_or_b32 s62, s39, s59
	s_lshl_b32 s62, s62, 12
	s_and_b32 s63, s62, 0x3f000
	s_or_b32 s63, s63, s58
	v_or_b32_e32 v2, s63, v231
	global_load_dwordx4 v[48:51], v2, s[6:7]
	global_load_dwordx4 v[52:55], v2, s[6:7] offset:1024
	global_load_dwordx4 v[56:59], v2, s[6:7] offset:2048
	global_load_dwordx4 v[60:63], v2, s[6:7] offset:3072
	s_add_i32 s63, s62, 0x4000
	s_and_b32 s63, s63, 0x3f000
	s_or_b32 s63, s63, s58
	v_or_b32_e32 v3, s63, v231
	global_load_dwordx4 v[40:43], v3, s[6:7] offset:2048
	global_load_dwordx4 v[44:47], v3, s[6:7] offset:3072
	s_add_i32 s63, s62, 0x6000
	s_and_b32 s63, s63, 0x3f000
	s_or_b32 s63, s63, s58
	v_or_b32_e32 v2, s63, v231
	global_load_dwordx4 v[148:151], v2, s[6:7] offset:3072
	s_add_i32 s63, s62, 0x7000
	s_and_b32 s63, s63, 0x3f000
	s_or_b32 s63, s63, s58
	v_or_b32_e32 v3, s63, v231
	global_load_dwordx4 v[132:135], v3, s[6:7]
	global_load_dwordx4 v[136:139], v3, s[6:7] offset:1024
	global_load_dwordx4 v[140:143], v3, s[6:7] offset:2048
	global_load_dwordx4 v[144:147], v3, s[6:7] offset:3072
	s_add_i32 s63, s62, 0x1000
	s_and_b32 s63, s63, 0x3f000
	s_or_b32 s63, s63, s58
	v_or_b32_e32 v2, s63, v231
	global_load_dwordx4 v[152:155], v2, s[6:7]
	global_load_dwordx4 v[156:159], v2, s[6:7] offset:1024
.Lka_done:
	s_add_i32 s63, s62, 0x4000
	s_and_b32 s63, s63, 0x3f000
	s_or_b32 s63, s63, s58
	v_or_b32_e32 v2, s63, v231
	global_load_dwordx4 v[32:35], v2, s[6:7]
	global_load_dwordx4 v[36:39], v2, s[6:7] offset:1024
	s_add_i32 s63, s62, 0x5000
	s_and_b32 s63, s63, 0x3f000
	s_or_b32 s63, s63, s58
	v_or_b32_e32 v3, s63, v231
	global_load_dwordx4 v[16:19], v3, s[6:7]
	global_load_dwordx4 v[20:23], v3, s[6:7] offset:1024
	global_load_dwordx4 v[24:27], v3, s[6:7] offset:2048
	global_load_dwordx4 v[28:31], v3, s[6:7] offset:3072
	s_add_i32 s63, s62, 0x6000
	s_and_b32 s63, s63, 0x3f000
	s_or_b32 s63, s63, s58
	v_or_b32_e32 v2, s63, v231
	global_load_dwordx4 v[4:7], v2, s[6:7]
	global_load_dwordx4 v[8:11], v2, s[6:7] offset:1024
	global_load_dwordx4 v[12:15], v2, s[6:7] offset:2048
	v_div_scale_f32 v1, s[64:65], v253, v253, v252
	v_rcp_f32_e32 v2, v1
	s_nop 0
	v_fma_f32 v0, -v1, v2, 1.0
	v_fmac_f32_e32 v2, v0, v2
	v_div_scale_f32 v0, vcc, v252, v253, v252
	v_mul_f32_e32 v3, v0, v2
	v_fma_f32 v248, -v1, v3, v0
	v_fmac_f32_e32 v3, v248, v2
	v_fma_f32 v0, -v1, v3, v0
	v_div_fmas_f32 v0, v0, v2, v3
	v_div_fixup_f32 v1, v0, v253, v252
	v_mul_f32_e32 v0, s18, v1
	v_mov_b32_e32 v2, s26
	v_mov_b32_e32 v3, s23
	v_cmp_eq_u32_e64 s[64:65], 0, v233
	v_cmp_eq_u32_e64 s[66:67], 1, v233
	v_cmp_eq_u32_e64 s[68:69], 2, v233
	v_cmp_eq_u32_e64 s[70:71], 3, v233
	v_cndmask_b32_e64 v248, v2, v3, s[64:65]
	v_cndmask_b32_e64 v249, v2, v3, s[66:67]
	v_cndmask_b32_e64 v250, v2, v3, s[68:69]
	v_cndmask_b32_e64 v251, v2, v3, s[70:71]
	v_mul_f32_e32 v248, v1, v248
	v_mul_f32_e32 v249, v1, v249
	v_mul_f32_e32 v250, v1, v250
	v_mul_f32_e32 v251, v1, v251
	v_cndmask_b32_e64 v248, v0, v248, s[2:3]
	v_cndmask_b32_e64 v249, v0, v249, s[2:3]
	v_cndmask_b32_e64 v250, v0, v250, s[2:3]
	v_cndmask_b32_e64 v251, v0, v251, s[2:3]
	v_mul_f32_e32 v248, v248, v208
	v_mul_f32_e32 v249, v249, v209
	v_mul_f32_e32 v250, v250, v204
	v_mul_f32_e32 v251, v251, v205
	ds_write_b128 v238, v[248:251]
	v_cmp_eq_u32_e64 s[64:65], 4, v233
	v_cmp_eq_u32_e64 s[66:67], 5, v233
	v_cmp_eq_u32_e64 s[68:69], 6, v233
	v_cmp_eq_u32_e64 s[70:71], 7, v233
	v_cndmask_b32_e64 v248, v2, v3, s[64:65]
	v_cndmask_b32_e64 v249, v2, v3, s[66:67]
	v_cndmask_b32_e64 v250, v2, v3, s[68:69]
	v_cndmask_b32_e64 v251, v2, v3, s[70:71]
	v_mul_f32_e32 v248, v1, v248
	v_mul_f32_e32 v249, v1, v249
	v_mul_f32_e32 v250, v1, v250
	v_mul_f32_e32 v251, v1, v251
	v_cndmask_b32_e64 v248, v0, v248, s[2:3]
	v_cndmask_b32_e64 v249, v0, v249, s[2:3]
	v_cndmask_b32_e64 v250, v0, v250, s[2:3]
	v_cndmask_b32_e64 v251, v0, v251, s[2:3]
	v_mul_f32_e32 v248, v248, v182
	v_mul_f32_e32 v249, v249, v183
	v_mul_f32_e32 v250, v250, v178
	v_mul_f32_e32 v251, v251, v179
	ds_write_b128 v238, v[248:251] offset:32
	v_cmp_eq_u32_e64 s[64:65], 8, v233
	v_cmp_eq_u32_e64 s[66:67], 9, v233
	v_cmp_eq_u32_e64 s[68:69], 10, v233
	v_cmp_eq_u32_e64 s[70:71], 11, v233
	v_cndmask_b32_e64 v248, v2, v3, s[64:65]
	v_cndmask_b32_e64 v249, v2, v3, s[66:67]
	v_cndmask_b32_e64 v250, v2, v3, s[68:69]
	v_cndmask_b32_e64 v251, v2, v3, s[70:71]
	v_mul_f32_e32 v248, v1, v248
	v_mul_f32_e32 v249, v1, v249
	v_mul_f32_e32 v250, v1, v250
	v_mul_f32_e32 v251, v1, v251
	v_cndmask_b32_e64 v248, v0, v248, s[2:3]
	v_cndmask_b32_e64 v249, v0, v249, s[2:3]
	v_cndmask_b32_e64 v250, v0, v250, s[2:3]
	v_cndmask_b32_e64 v251, v0, v251, s[2:3]
	v_mul_f32_e32 v248, v248, v166
	v_mul_f32_e32 v249, v249, v167
	v_mul_f32_e32 v250, v250, v118
	v_mul_f32_e32 v251, v251, v119
	ds_write_b128 v238, v[248:251] offset:64
	v_cmp_eq_u32_e64 s[64:65], 12, v233
	v_cmp_eq_u32_e64 s[66:67], 13, v233
	v_cmp_eq_u32_e64 s[68:69], 14, v233
	v_cmp_eq_u32_e64 s[70:71], 15, v233
	v_cndmask_b32_e64 v248, v2, v3, s[64:65]
	v_cndmask_b32_e64 v249, v2, v3, s[66:67]
	v_cndmask_b32_e64 v250, v2, v3, s[68:69]
	v_cndmask_b32_e64 v251, v2, v3, s[70:71]
	v_mul_f32_e32 v248, v1, v248
	v_mul_f32_e32 v249, v1, v249
	v_mul_f32_e32 v250, v1, v250
	v_mul_f32_e32 v251, v1, v251
	v_cndmask_b32_e64 v248, v0, v248, s[2:3]
	v_cndmask_b32_e64 v249, v0, v249, s[2:3]
	v_cndmask_b32_e64 v250, v0, v250, s[2:3]
	v_cndmask_b32_e64 v251, v0, v251, s[2:3]
	v_mul_f32_e32 v248, v248, v116
	v_mul_f32_e32 v249, v249, v117
	v_mul_f32_e32 v250, v250, v114
	v_mul_f32_e32 v251, v251, v115
	ds_write_b128 v238, v[248:251] offset:96
	v_pk_mul_f32 v[248:249], v[0:1], v[112:113] op_sel_hi:[0,1]
	v_pk_mul_f32 v[250:251], v[0:1], v[98:99] op_sel_hi:[0,1]
	ds_write_b128 v238, v[248:251] offset:128
	v_pk_mul_f32 v[248:249], v[0:1], v[100:101] op_sel_hi:[0,1]
	v_pk_mul_f32 v[250:251], v[0:1], v[120:121] op_sel_hi:[0,1]
	ds_write_b128 v238, v[248:251] offset:160
	v_pk_mul_f32 v[248:249], v[0:1], v[102:103] op_sel_hi:[0,1]
	v_pk_mul_f32 v[250:251], v[0:1], v[122:123] op_sel_hi:[0,1]
	ds_write_b128 v238, v[248:251] offset:192
	v_pk_mul_f32 v[248:249], v[0:1], v[124:125] op_sel_hi:[0,1]
	v_pk_mul_f32 v[250:251], v[0:1], v[180:181] op_sel_hi:[0,1]
	ds_write_b128 v238, v[248:251] offset:224
	s_lshl_b32 s56, s56, 11
	s_add_i32 s56, s56, s25
	v_or_b32_e32 v252, s56, v239
	v_add_lshl_u32 v253, v241, s55, 7
	v_lshl_or_b32 v1, v252, 13, v240
	v_and_or_b32 v2, v253, s54, v1
	ds_read_b128 v[248:251], v246
	ds_read_b128 v[160:163], v246 offset:1088
	s_waitcnt lgkmcnt(1)
	global_store_dwordx4 v2, v[248:251], s[10:11] nt
	s_nop 0
	ds_read_b128 v[248:251], v246 offset:2176
	v_or_b32_e32 v3, 0x8000, v2
	s_waitcnt lgkmcnt(1)
	global_store_dwordx4 v3, v[160:163], s[10:11] nt
	s_nop 0
	ds_read_b128 v[160:163], v246 offset:3264
	v_or_b32_e32 v252, 0x10000, v2
	s_waitcnt lgkmcnt(1)
	global_store_dwordx4 v252, v[248:251], s[10:11] nt
	s_nop 0
	ds_read_b128 v[248:251], v246 offset:4352
	v_or_b32_e32 v3, 0x18000, v2
	s_waitcnt lgkmcnt(1)
	global_store_dwordx4 v3, v[160:163], s[10:11] nt
	s_nop 0
	ds_read_b128 v[160:163], v246 offset:5440
	v_or_b32_e32 v252, 0x20000, v2
	s_waitcnt lgkmcnt(1)
	global_store_dwordx4 v252, v[248:251], s[10:11] nt
	s_nop 0
	ds_read_b128 v[248:251], v246 offset:6528
	v_or_b32_e32 v3, 0x28000, v2
	s_waitcnt lgkmcnt(1)
	global_store_dwordx4 v3, v[160:163], s[10:11] nt
	s_nop 0
	ds_read_b128 v[160:163], v246 offset:7616
	v_or_b32_e32 v252, 0x30000, v2
	s_waitcnt lgkmcnt(1)
	global_store_dwordx4 v252, v[248:251], s[10:11] nt
	v_or_b32_e32 v3, 0x38000, v2
	s_waitcnt lgkmcnt(0)
	global_store_dwordx4 v3, v[160:163], s[10:11] nt
	v_pk_mul_f32 v[248:249], v[0:1], v[80:81] op_sel_hi:[0,1]
	v_pk_mul_f32 v[250:251], v[0:1], v[82:83] op_sel_hi:[0,1]
	ds_write_b128 v238, v[248:251]
	v_pk_mul_f32 v[248:249], v[0:1], v[84:85] op_sel_hi:[0,1]
	v_pk_mul_f32 v[250:251], v[0:1], v[96:97] op_sel_hi:[0,1]
	ds_write_b128 v238, v[248:251] offset:32
	v_pk_mul_f32 v[248:249], v[0:1], v[86:87] op_sel_hi:[0,1]
	v_pk_mul_f32 v[250:251], v[0:1], v[88:89] op_sel_hi:[0,1]
	ds_write_b128 v238, v[248:251] offset:64
	v_pk_mul_f32 v[248:249], v[0:1], v[90:91] op_sel_hi:[0,1]
	v_pk_mul_f32 v[250:251], v[0:1], v[94:95] op_sel_hi:[0,1]
	ds_write_b128 v238, v[248:251] offset:96
	v_pk_mul_f32 v[248:249], v[0:1], v[92:93] op_sel_hi:[0,1]
	v_pk_mul_f32 v[250:251], v[0:1], v[108:109] op_sel_hi:[0,1]
	ds_write_b128 v238, v[248:251] offset:128
	v_pk_mul_f32 v[248:249], v[0:1], v[110:111] op_sel_hi:[0,1]
	v_pk_mul_f32 v[250:251], v[0:1], v[176:177] op_sel_hi:[0,1]
	ds_write_b128 v238, v[248:251] offset:160
	v_pk_mul_f32 v[248:249], v[0:1], v[174:175] op_sel_hi:[0,1]
	v_pk_mul_f32 v[250:251], v[0:1], v[192:193] op_sel_hi:[0,1]
	ds_write_b128 v238, v[248:251] offset:192
	v_pk_mul_f32 v[248:249], v[0:1], v[194:195] op_sel_hi:[0,1]
	v_pk_mul_f32 v[250:251], v[0:1], v[206:207] op_sel_hi:[0,1]
	ds_write_b128 v238, v[248:251] offset:224
	v_add_u32_e32 v252, 0x100, v253
	v_and_or_b32 v2, v252, s54, v1
	ds_read_b128 v[248:251], v246
	ds_read_b128 v[160:163], v246 offset:1088
	s_waitcnt lgkmcnt(1)
	global_store_dwordx4 v2, v[248:251], s[10:11] nt
	s_nop 0
	ds_read_b128 v[248:251], v246 offset:2176
	v_or_b32_e32 v3, 0x8000, v2
	s_waitcnt lgkmcnt(1)
	global_store_dwordx4 v3, v[160:163], s[10:11] nt
	s_nop 0
	ds_read_b128 v[160:163], v246 offset:3264
	v_or_b32_e32 v252, 0x10000, v2
	s_waitcnt lgkmcnt(1)
	global_store_dwordx4 v252, v[248:251], s[10:11] nt
	s_nop 0
	ds_read_b128 v[248:251], v246 offset:4352
	v_or_b32_e32 v3, 0x18000, v2
	s_waitcnt lgkmcnt(1)
	global_store_dwordx4 v3, v[160:163], s[10:11] nt
	s_nop 0
	ds_read_b128 v[160:163], v246 offset:5440
	v_or_b32_e32 v252, 0x20000, v2
	s_waitcnt lgkmcnt(1)
	global_store_dwordx4 v252, v[248:251], s[10:11] nt
	s_nop 0
	ds_read_b128 v[248:251], v246 offset:6528
	v_or_b32_e32 v3, 0x28000, v2
	s_waitcnt lgkmcnt(1)
	global_store_dwordx4 v3, v[160:163], s[10:11] nt
	s_nop 0
	ds_read_b128 v[160:163], v246 offset:7616
	v_or_b32_e32 v252, 0x30000, v2
	s_waitcnt lgkmcnt(1)
	global_store_dwordx4 v252, v[248:251], s[10:11] nt
	v_or_b32_e32 v3, 0x38000, v2
	s_waitcnt lgkmcnt(0)
	global_store_dwordx4 v3, v[160:163], s[10:11] nt
	s_add_i32 s63, s62, 0x3000
	s_and_b32 s63, s63, 0x3f000
	s_or_b32 s63, s63, s58
	v_or_b32_e32 v2, s63, v231
	global_load_dwordx4 v[80:83], v2, s[6:7]
	global_load_dwordx4 v[84:87], v2, s[6:7] offset:1024
	global_load_dwordx4 v[88:91], v2, s[6:7] offset:2048
	global_load_dwordx4 v[92:95], v2, s[6:7] offset:3072
	s_add_i32 s63, s62, 0x2000
	s_and_b32 s63, s63, 0x3f000
	s_or_b32 s63, s63, s58
	v_or_b32_e32 v3, s63, v231
	global_load_dwordx4 v[96:99], v3, s[6:7]
	global_load_dwordx4 v[100:103], v3, s[6:7] offset:1024
	global_load_dwordx4 v[108:111], v3, s[6:7] offset:2048
	global_load_dwordx4 v[192:195], v3, s[6:7] offset:3072
	s_add_i32 s63, s62, 0x1000
	s_and_b32 s63, s63, 0x3f000
	s_or_b32 s63, s63, s58
	v_or_b32_e32 v2, s63, v231
	global_load_dwordx4 v[174:177], v2, s[6:7] offset:2048
	global_load_dwordx4 v[178:181], v2, s[6:7] offset:3072
	v_pk_mul_f32 v[248:249], v[0:1], v[64:65] op_sel_hi:[0,1]
	v_pk_mul_f32 v[250:251], v[0:1], v[66:67] op_sel_hi:[0,1]
	ds_write_b128 v238, v[248:251]
	v_pk_mul_f32 v[248:249], v[0:1], v[68:69] op_sel_hi:[0,1]
	v_pk_mul_f32 v[250:251], v[0:1], v[74:75] op_sel_hi:[0,1]
	ds_write_b128 v238, v[248:251] offset:32
	v_pk_mul_f32 v[248:249], v[0:1], v[72:73] op_sel_hi:[0,1]
	v_pk_mul_f32 v[250:251], v[0:1], v[104:105] op_sel_hi:[0,1]
	ds_write_b128 v238, v[248:251] offset:64
	v_pk_mul_f32 v[248:249], v[0:1], v[106:107] op_sel_hi:[0,1]
	v_pk_mul_f32 v[250:251], v[0:1], v[172:173] op_sel_hi:[0,1]
	ds_write_b128 v238, v[248:251] offset:96
	v_pk_mul_f32 v[248:249], v[0:1], v[170:171] op_sel_hi:[0,1]
	v_pk_mul_f32 v[250:251], v[0:1], v[188:189] op_sel_hi:[0,1]
	ds_write_b128 v238, v[248:251] offset:128
	v_pk_mul_f32 v[248:249], v[0:1], v[190:191] op_sel_hi:[0,1]
	v_pk_mul_f32 v[250:251], v[0:1], v[202:203] op_sel_hi:[0,1]
	ds_write_b128 v238, v[248:251] offset:160
	v_pk_mul_f32 v[248:249], v[0:1], v[200:201] op_sel_hi:[0,1]
	v_pk_mul_f32 v[250:251], v[0:1], v[214:215] op_sel_hi:[0,1]
	ds_write_b128 v238, v[248:251] offset:192
	v_pk_mul_f32 v[248:249], v[0:1], v[216:217] op_sel_hi:[0,1]
	v_pk_mul_f32 v[250:251], v[0:1], v[222:223] op_sel_hi:[0,1]
	ds_write_b128 v238, v[248:251] offset:224
	v_add_u32_e32 v252, 0x200, v253
	v_and_or_b32 v2, v252, s54, v1
	ds_read_b128 v[248:251], v246
	ds_read_b128 v[160:163], v246 offset:1088
	s_waitcnt lgkmcnt(1)
	global_store_dwordx4 v2, v[248:251], s[10:11] nt
	s_nop 0
	ds_read_b128 v[248:251], v246 offset:2176
	v_or_b32_e32 v3, 0x8000, v2
	s_waitcnt lgkmcnt(1)
	global_store_dwordx4 v3, v[160:163], s[10:11] nt
	s_nop 0
	ds_read_b128 v[160:163], v246 offset:3264
	v_or_b32_e32 v252, 0x10000, v2
	s_waitcnt lgkmcnt(1)
	global_store_dwordx4 v252, v[248:251], s[10:11] nt
	s_nop 0
	ds_read_b128 v[248:251], v246 offset:4352
	v_or_b32_e32 v3, 0x18000, v2
	s_waitcnt lgkmcnt(1)
	global_store_dwordx4 v3, v[160:163], s[10:11] nt
	s_nop 0
	ds_read_b128 v[160:163], v246 offset:5440
	v_or_b32_e32 v252, 0x20000, v2
	s_waitcnt lgkmcnt(1)
	global_store_dwordx4 v252, v[248:251], s[10:11] nt
	s_nop 0
	ds_read_b128 v[248:251], v246 offset:6528
	v_or_b32_e32 v3, 0x28000, v2
	s_waitcnt lgkmcnt(1)
	global_store_dwordx4 v3, v[160:163], s[10:11] nt
	s_nop 0
	ds_read_b128 v[160:163], v246 offset:7616
	v_or_b32_e32 v252, 0x30000, v2
	s_waitcnt lgkmcnt(1)
	global_store_dwordx4 v252, v[248:251], s[10:11] nt
	v_or_b32_e32 v3, 0x38000, v2
	s_waitcnt lgkmcnt(0)
	global_store_dwordx4 v3, v[160:163], s[10:11] nt
	v_pk_mul_f32 v[248:249], v[0:1], v[70:71] op_sel_hi:[0,1]
	v_pk_mul_f32 v[250:251], v[0:1], v[76:77] op_sel_hi:[0,1]
	ds_write_b128 v238, v[248:251]
	v_pk_mul_f32 v[248:249], v[0:1], v[78:79] op_sel_hi:[0,1]
	v_pk_mul_f32 v[250:251], v[0:1], v[168:169] op_sel_hi:[0,1]
	ds_write_b128 v238, v[248:251] offset:32
	v_pk_mul_f32 v[248:249], v[0:1], v[126:127] op_sel_hi:[0,1]
	v_pk_mul_f32 v[250:251], v[0:1], v[184:185] op_sel_hi:[0,1]
	ds_write_b128 v238, v[248:251] offset:64
	v_pk_mul_f32 v[248:249], v[0:1], v[186:187] op_sel_hi:[0,1]
	v_pk_mul_f32 v[250:251], v[0:1], v[198:199] op_sel_hi:[0,1]
	ds_write_b128 v238, v[248:251] offset:96
	v_pk_mul_f32 v[248:249], v[0:1], v[196:197] op_sel_hi:[0,1]
	v_pk_mul_f32 v[250:251], v[0:1], v[210:211] op_sel_hi:[0,1]
	ds_write_b128 v238, v[248:251] offset:128
	v_pk_mul_f32 v[248:249], v[0:1], v[212:213] op_sel_hi:[0,1]
	v_pk_mul_f32 v[250:251], v[0:1], v[220:221] op_sel_hi:[0,1]
	ds_write_b128 v238, v[248:251] offset:160
	v_pk_mul_f32 v[248:249], v[0:1], v[218:219] op_sel_hi:[0,1]
	v_pk_mul_f32 v[250:251], v[0:1], v[224:225] op_sel_hi:[0,1]
	ds_write_b128 v238, v[248:251] offset:192
	v_pk_mul_f32 v[248:249], v[0:1], v[226:227] op_sel_hi:[0,1]
	v_pk_mul_f32 v[250:251], v[0:1], v[228:229] op_sel_hi:[0,1]
	ds_write_b128 v238, v[248:251] offset:224
	v_add_u32_e32 v252, 0x300, v253
	v_and_or_b32 v2, v252, s54, v1
	ds_read_b128 v[248:251], v246
	ds_read_b128 v[160:163], v246 offset:1088
	s_waitcnt lgkmcnt(1)
	global_store_dwordx4 v2, v[248:251], s[10:11] nt
	s_nop 0
	ds_read_b128 v[248:251], v246 offset:2176
	v_or_b32_e32 v3, 0x8000, v2
	s_waitcnt lgkmcnt(1)
	global_store_dwordx4 v3, v[160:163], s[10:11] nt
	s_nop 0
	ds_read_b128 v[160:163], v246 offset:3264
	v_or_b32_e32 v252, 0x10000, v2
	s_waitcnt lgkmcnt(1)
	global_store_dwordx4 v252, v[248:251], s[10:11] nt
	s_nop 0
	ds_read_b128 v[248:251], v246 offset:4352
	v_or_b32_e32 v3, 0x18000, v2
	s_waitcnt lgkmcnt(1)
	global_store_dwordx4 v3, v[160:163], s[10:11] nt
	s_nop 0
	ds_read_b128 v[160:163], v246 offset:5440
	v_or_b32_e32 v252, 0x20000, v2
	s_waitcnt lgkmcnt(1)
	global_store_dwordx4 v252, v[248:251], s[10:11] nt
	s_nop 0
	ds_read_b128 v[248:251], v246 offset:6528
	v_or_b32_e32 v3, 0x28000, v2
	s_waitcnt lgkmcnt(1)
	global_store_dwordx4 v3, v[160:163], s[10:11] nt
	s_nop 0
	ds_read_b128 v[160:163], v246 offset:7616
	v_or_b32_e32 v252, 0x30000, v2
	s_waitcnt lgkmcnt(1)
	global_store_dwordx4 v252, v[248:251], s[10:11] nt
	v_or_b32_e32 v3, 0x38000, v2
	s_waitcnt lgkmcnt(0)
	global_store_dwordx4 v3, v[160:163], s[10:11] nt
	s_mov_b32 s57, s24
	s_add_i32 s12, s12, 4
	s_cmp_eq_u32 s12, 32
	s_cbranch_scc1 .LBB1_22
